# first K-tile MFMAs take srcC=0 (no accumulator zero-inits) in the four fp8 GEMM phases
# speedup vs baseline: 1.0072x; 1.0022x over previous
.LBB0_238:
	s_and_b64 s[10:11], s[30:31], exec
	s_cselect_b32 s65, s27, s37
	s_cselect_b32 s84, s26, s36
	s_cselect_b32 s85, s29, s35
	s_cselect_b32 s86, s28, s34
	s_add_u32 s9, s36, 0x100
	s_addc_u32 s10, s37, 0
	s_add_u32 s11, s34, 0x100
	s_addc_u32 s42, s35, 0
	s_waitcnt lgkmcnt(0)
	s_cmp_eq_u32 s81, 2
	s_cselect_b32 s39, s65, s10
	s_cselect_b32 s38, s84, s9
	s_cselect_b32 s43, s85, s42
	s_cselect_b32 s42, s86, s11
	s_barrier
	s_setprio 1
	s_mov_b32 s10, s8
	s_mov_b32 s11, s8
	s_mov_b32 s9, s8
	s_waitcnt lgkmcnt(0)
	v_mfma_scale_f32_16x16x128_f8f6f4 v[70:73], v[26:33], v[58:65], 0, v1, v200 op_sel_hi:[0,0,0]
	v_mfma_scale_f32_16x16x128_f8f6f4 v[86:89], v[18:25], v[58:65], 0, v1, v200 op_sel_hi:[0,0,0]
	v_mfma_scale_f32_16x16x128_f8f6f4 v[74:77], v[26:33], v[50:57], 0, v1, v200 op_sel_hi:[0,0,0]
	v_mfma_scale_f32_16x16x128_f8f6f4 v[90:93], v[18:25], v[50:57], 0, v1, v200 op_sel_hi:[0,0,0]
	v_mfma_scale_f32_16x16x128_f8f6f4 v[78:81], v[26:33], v[42:49], 0, v1, v200 op_sel_hi:[0,0,0]
	v_mfma_scale_f32_16x16x128_f8f6f4 v[94:97], v[18:25], v[42:49], 0, v1, v200 op_sel_hi:[0,0,0]
	v_mfma_scale_f32_16x16x128_f8f6f4 v[82:85], v[26:33], v[34:41], 0, v1, v200 op_sel_hi:[0,0,0]
	v_mfma_scale_f32_16x16x128_f8f6f4 v[98:101], v[18:25], v[34:41], 0, v1, v200 op_sel_hi:[0,0,0]
	s_setprio 0
	s_setprio 1
	v_mfma_scale_f32_16x16x128_f8f6f4 v[114:117], v[10:17], v[58:65], 0, v1, v200 op_sel_hi:[0,0,0]
	v_mfma_scale_f32_16x16x128_f8f6f4 v[126:129], v[2:9], v[58:65], 0, v1, v200 op_sel_hi:[0,0,0]
	v_mfma_scale_f32_16x16x128_f8f6f4 v[118:121], v[10:17], v[50:57], 0, v1, v200 op_sel_hi:[0,0,0]
	v_mfma_scale_f32_16x16x128_f8f6f4 v[122:125], v[2:9], v[50:57], 0, v1, v200 op_sel_hi:[0,0,0]
	v_mfma_scale_f32_16x16x128_f8f6f4 v[106:109], v[10:17], v[42:49], 0, v1, v200 op_sel_hi:[0,0,0]
	v_mfma_scale_f32_16x16x128_f8f6f4 v[110:113], v[2:9], v[42:49], 0, v1, v200 op_sel_hi:[0,0,0]
	v_mfma_scale_f32_16x16x128_f8f6f4 v[102:105], v[10:17], v[34:41], 0, v1, v200 op_sel_hi:[0,0,0]
	v_mfma_scale_f32_16x16x128_f8f6f4 v[66:69], v[2:9], v[34:41], 0, v1, v200 op_sel_hi:[0,0,0]
	s_setprio 0
	s_barrier
	s_mov_b32 m0, s51
	v_lshl_add_u64 v[198:199], s[42:43], 0, v[178:179]
	ds_read_b128 v[58:61], v206 offset:16384
	ds_read_b128 v[62:65], v206 offset:17408
	ds_read_b128 v[50:53], v206 offset:18432
	ds_read_b128 v[54:57], v206 offset:19456
	ds_read_b128 v[42:45], v206 offset:20480
	ds_read_b128 v[46:49], v206 offset:21504
	ds_read_b128 v[34:37], v206 offset:22528
	ds_read_b128 v[38:41], v206 offset:23552
	global_load_lds_dwordx4 v[198:199], off
	v_lshl_add_u64 v[196:197], s[42:43], 0, v[174:175]
	s_mov_b32 m0, s58
	v_lshl_add_u64 v[194:195], s[42:43], 0, v[180:181]
	global_load_lds_dwordx4 v[196:197], off
	s_mov_b32 m0, s59
	v_lshl_add_u64 v[192:193], s[42:43], 0, v[176:177]
	global_load_lds_dwordx4 v[194:195], off
	s_mov_b32 m0, s60
	v_lshl_add_u64 v[188:189], s[38:39], 0, v[178:179]
	global_load_lds_dwordx4 v[192:193], off
	s_mov_b32 m0, s50
	v_lshl_add_u64 v[190:191], s[38:39], 0, v[174:175]
	global_load_lds_dwordx4 v[188:189], off
	s_mov_b32 m0, s61
	s_and_b64 vcc, exec, s[40:41]
	global_load_lds_dwordx4 v[190:191], off
	s_cbranch_vccz .LBB0_251
	s_waitcnt vmcnt(24)
	s_cbranch_execnz .LBB0_241

.LBB0_241:
	s_waitcnt lgkmcnt(0)
	s_barrier
	s_setprio 1
	s_mov_b32 s10, s8
	s_mov_b32 s11, s8
	s_mov_b32 s9, s8
	s_waitcnt lgkmcnt(0)
	v_mfma_scale_f32_16x16x128_f8f6f4 v[134:137], v[26:33], v[58:65], 0, v1, v200 op_sel_hi:[0,0,0]
	v_mfma_scale_f32_16x16x128_f8f6f4 v[142:145], v[18:25], v[58:65], 0, v1, v200 op_sel_hi:[0,0,0]
	v_mfma_scale_f32_16x16x128_f8f6f4 v[138:141], v[26:33], v[50:57], 0, v1, v200 op_sel_hi:[0,0,0]
	v_mfma_scale_f32_16x16x128_f8f6f4 v[150:153], v[18:25], v[50:57], 0, v1, v200 op_sel_hi:[0,0,0]
	v_mfma_scale_f32_16x16x128_f8f6f4 v[146:149], v[26:33], v[42:49], 0, v1, v200 op_sel_hi:[0,0,0]
	v_mfma_scale_f32_16x16x128_f8f6f4 v[158:161], v[18:25], v[42:49], 0, v1, v200 op_sel_hi:[0,0,0]
	v_mfma_scale_f32_16x16x128_f8f6f4 v[154:157], v[26:33], v[34:41], 0, v1, v200 op_sel_hi:[0,0,0]
	v_mfma_scale_f32_16x16x128_f8f6f4 v[162:165], v[18:25], v[34:41], 0, v1, v200 op_sel_hi:[0,0,0]
	s_setprio 0
	s_setprio 1
	v_mfma_scale_f32_16x16x128_f8f6f4 v[166:169], v[10:17], v[58:65], 0, v1, v200 op_sel_hi:[0,0,0]
	v_mfma_scale_f32_16x16x128_f8f6f4 v[170:173], v[2:9], v[58:65], 0, v1, v200 op_sel_hi:[0,0,0]
	v_mfma_scale_f32_16x16x128_f8f6f4 v[58:61], v[10:17], v[50:57], 0, v1, v200 op_sel_hi:[0,0,0]
	v_mfma_scale_f32_16x16x128_f8f6f4 v[62:65], v[2:9], v[50:57], 0, v1, v200 op_sel_hi:[0,0,0]
	v_mfma_scale_f32_16x16x128_f8f6f4 v[50:53], v[10:17], v[42:49], 0, v1, v200 op_sel_hi:[0,0,0]
	v_mfma_scale_f32_16x16x128_f8f6f4 v[54:57], v[2:9], v[42:49], 0, v1, v200 op_sel_hi:[0,0,0]
	v_mfma_scale_f32_16x16x128_f8f6f4 v[42:45], v[10:17], v[34:41], 0, v1, v200 op_sel_hi:[0,0,0]
	v_mfma_scale_f32_16x16x128_f8f6f4 v[130:133], v[2:9], v[34:41], 0, v1, v200 op_sel_hi:[0,0,0]
	s_setprio 0
	s_barrier
	s_add_i32 s9, 0, 0x18000
	s_add_i32 s10, 0, 0x1c000
	v_add_u32_e32 v182, s9, v202
	v_add_u32_e32 v207, s10, v202
	ds_read_b128 v[26:29], v182
	ds_read_b128 v[30:33], v182 offset:1024
	ds_read_b128 v[18:21], v182 offset:2048
	ds_read_b128 v[22:25], v182 offset:3072
	ds_read_b128 v[10:13], v207
	ds_read_b128 v[14:17], v207 offset:1024
	ds_read_b128 v[2:5], v207 offset:2048
	ds_read_b128 v[6:9], v207 offset:3072
	s_mov_b32 m0, s62
	v_lshl_add_u64 v[46:47], s[38:39], 0, v[180:181]
	ds_read_b128 v[34:37], v206 offset:32768
	ds_read_b128 v[38:41], v206 offset:33792
	ds_read_b128 v[208:211], v206 offset:34816
	ds_read_b128 v[212:215], v206 offset:35840
	ds_read_b128 v[216:219], v206 offset:36864
	ds_read_b128 v[220:223], v206 offset:37888
	ds_read_b128 v[224:227], v206 offset:38912
	ds_read_b128 v[228:231], v206 offset:39936
	global_load_lds_dwordx4 v[46:47], off
	v_lshl_add_u64 v[46:47], s[38:39], 0, v[176:177]
	s_mov_b32 m0, s63
	s_nop 0
	global_load_lds_dwordx4 v[46:47], off
	s_waitcnt vmcnt(8)
	s_waitcnt lgkmcnt(0)
	s_barrier
	s_setprio 1
	s_waitcnt lgkmcnt(0)
	v_mfma_scale_f32_16x16x128_f8f6f4 v[70:73], v[26:33], v[34:41], v[70:73], v1, v200 op_sel_hi:[0,0,0]
	v_mfma_scale_f32_16x16x128_f8f6f4 v[86:89], v[18:25], v[34:41], v[86:89], v1, v200 op_sel_hi:[0,0,0]
	v_mfma_scale_f32_16x16x128_f8f6f4 v[74:77], v[26:33], v[208:215], v[74:77], v1, v200 op_sel_hi:[0,0,0]
	v_mfma_scale_f32_16x16x128_f8f6f4 v[90:93], v[18:25], v[208:215], v[90:93], v1, v200 op_sel_hi:[0,0,0]
	v_mfma_scale_f32_16x16x128_f8f6f4 v[78:81], v[26:33], v[216:223], v[78:81], v1, v200 op_sel_hi:[0,0,0]
	v_mfma_scale_f32_16x16x128_f8f6f4 v[94:97], v[18:25], v[216:223], v[94:97], v1, v200 op_sel_hi:[0,0,0]
	v_mfma_scale_f32_16x16x128_f8f6f4 v[82:85], v[26:33], v[224:231], v[82:85], v1, v200 op_sel_hi:[0,0,0]
	v_mfma_scale_f32_16x16x128_f8f6f4 v[98:101], v[18:25], v[224:231], v[98:101], v1, v200 op_sel_hi:[0,0,0]
	s_setprio 0
	s_setprio 1
	v_mfma_scale_f32_16x16x128_f8f6f4 v[114:117], v[10:17], v[34:41], v[114:117], v1, v200 op_sel_hi:[0,0,0]
	v_mfma_scale_f32_16x16x128_f8f6f4 v[126:129], v[2:9], v[34:41], v[126:129], v1, v200 op_sel_hi:[0,0,0]
	v_mfma_scale_f32_16x16x128_f8f6f4 v[118:121], v[10:17], v[208:215], v[118:121], v1, v200 op_sel_hi:[0,0,0]
	v_mfma_scale_f32_16x16x128_f8f6f4 v[122:125], v[2:9], v[208:215], v[122:125], v1, v200 op_sel_hi:[0,0,0]
	v_mfma_scale_f32_16x16x128_f8f6f4 v[106:109], v[10:17], v[216:223], v[106:109], v1, v200 op_sel_hi:[0,0,0]
	v_mfma_scale_f32_16x16x128_f8f6f4 v[110:113], v[2:9], v[216:223], v[110:113], v1, v200 op_sel_hi:[0,0,0]
	v_mfma_scale_f32_16x16x128_f8f6f4 v[102:105], v[10:17], v[224:231], v[102:105], v1, v200 op_sel_hi:[0,0,0]
	v_mfma_scale_f32_16x16x128_f8f6f4 v[66:69], v[2:9], v[224:231], v[66:69], v1, v200 op_sel_hi:[0,0,0]
	s_setprio 0
	s_barrier
	s_add_i32 s9, s9, s48
	v_lshl_add_u64 v[46:47], v[198:199], 0, s[12:13]
	s_mov_b32 m0, s9
	s_add_i32 s38, s9, 0x2000
	ds_read_b128 v[34:37], v206 offset:49152
	ds_read_b128 v[38:41], v206 offset:50176
	ds_read_b128 v[208:211], v206 offset:51200
	ds_read_b128 v[212:215], v206 offset:52224
	ds_read_b128 v[216:219], v206 offset:53248
	ds_read_b128 v[220:223], v206 offset:54272
	ds_read_b128 v[224:227], v206 offset:55296
	ds_read_b128 v[228:231], v206 offset:56320
	global_load_lds_dwordx4 v[46:47], off
	v_lshl_add_u64 v[46:47], v[196:197], 0, s[12:13]
	s_mov_b32 m0, s38
	s_add_i32 s39, s10, s48
	global_load_lds_dwordx4 v[46:47], off
	v_lshl_add_u64 v[46:47], v[194:195], 0, s[12:13]
	s_mov_b32 m0, s39
	s_add_i32 s40, s39, 0x2000
	global_load_lds_dwordx4 v[46:47], off
	v_lshl_add_u64 v[46:47], v[192:193], 0, s[12:13]
	s_mov_b32 m0, s40
	s_nop 0
	global_load_lds_dwordx4 v[46:47], off
	v_lshl_add_u64 v[46:47], v[188:189], 0, s[12:13]
	s_mov_b32 m0, s71
	s_nop 0
	global_load_lds_dwordx4 v[46:47], off
	v_lshl_add_u64 v[46:47], v[190:191], 0, s[12:13]
	s_mov_b32 m0, s72
	s_nop 0
	global_load_lds_dwordx4 v[46:47], off
	s_waitcnt vmcnt(8)
	s_waitcnt lgkmcnt(0)
	s_barrier
	s_setprio 1
	s_waitcnt lgkmcnt(0)
	v_mfma_scale_f32_16x16x128_f8f6f4 v[134:137], v[26:33], v[34:41], v[134:137], v1, v200 op_sel_hi:[0,0,0]
	v_mfma_scale_f32_16x16x128_f8f6f4 v[142:145], v[18:25], v[34:41], v[142:145], v1, v200 op_sel_hi:[0,0,0]
	v_mfma_scale_f32_16x16x128_f8f6f4 v[138:141], v[26:33], v[208:215], v[138:141], v1, v200 op_sel_hi:[0,0,0]
	v_mfma_scale_f32_16x16x128_f8f6f4 v[150:153], v[18:25], v[208:215], v[150:153], v1, v200 op_sel_hi:[0,0,0]
	v_mfma_scale_f32_16x16x128_f8f6f4 v[146:149], v[26:33], v[216:223], v[146:149], v1, v200 op_sel_hi:[0,0,0]
	v_mfma_scale_f32_16x16x128_f8f6f4 v[158:161], v[18:25], v[216:223], v[158:161], v1, v200 op_sel_hi:[0,0,0]
	v_mfma_scale_f32_16x16x128_f8f6f4 v[154:157], v[26:33], v[224:231], v[154:157], v1, v200 op_sel_hi:[0,0,0]
	v_mfma_scale_f32_16x16x128_f8f6f4 v[162:165], v[18:25], v[224:231], v[162:165], v1, v200 op_sel_hi:[0,0,0]
	s_setprio 0
	s_setprio 1
	v_mfma_scale_f32_16x16x128_f8f6f4 v[166:169], v[10:17], v[34:41], v[166:169], v1, v200 op_sel_hi:[0,0,0]
	v_mfma_scale_f32_16x16x128_f8f6f4 v[170:173], v[2:9], v[34:41], v[170:173], v1, v200 op_sel_hi:[0,0,0]
	v_mfma_scale_f32_16x16x128_f8f6f4 v[58:61], v[10:17], v[208:215], v[58:61], v1, v200 op_sel_hi:[0,0,0]
	v_mfma_scale_f32_16x16x128_f8f6f4 v[62:65], v[2:9], v[208:215], v[62:65], v1, v200 op_sel_hi:[0,0,0]
	v_mfma_scale_f32_16x16x128_f8f6f4 v[50:53], v[10:17], v[216:223], v[50:53], v1, v200 op_sel_hi:[0,0,0]
	v_mfma_scale_f32_16x16x128_f8f6f4 v[54:57], v[2:9], v[216:223], v[54:57], v1, v200 op_sel_hi:[0,0,0]
	v_mfma_scale_f32_16x16x128_f8f6f4 v[42:45], v[10:17], v[224:231], v[42:45], v1, v200 op_sel_hi:[0,0,0]
	v_mfma_scale_f32_16x16x128_f8f6f4 v[130:133], v[2:9], v[224:231], v[130:133], v1, v200 op_sel_hi:[0,0,0]
	s_setprio 0
	s_barrier
	s_cmp_lt_u32 s81, 3
	s_cbranch_scc1 .LBB0_244
	s_add_u32 s10, s36, 0x180
	s_addc_u32 s11, s37, 0
	s_add_u32 s41, s34, 0x200
	s_addc_u32 s42, s35, 0
	s_mov_b32 s43, 4

.LBB0_680:
	s_add_u32 s5, s34, 0x100
	s_addc_u32 s27, s35, 0
	s_and_b64 s[6:7], s[18:19], exec
	s_cselect_b32 s39, s29, s27
	s_cselect_b32 s38, s28, s5
	s_add_u32 s5, s36, 0x100
	s_waitcnt lgkmcnt(0)
	s_addc_u32 s27, s37, 0
	s_and_b64 s[6:7], s[18:19], exec
	s_cselect_b32 s43, s31, s27
	s_cselect_b32 s42, s30, s5
	s_barrier
	s_setprio 1
	s_mov_b32 s6, s4
	s_mov_b32 s7, s4
	s_mov_b32 s5, s4
	s_waitcnt lgkmcnt(0)
	v_mfma_scale_f32_16x16x128_f8f6f4 v[70:73], v[26:33], v[58:65], 0, v1, v198 op_sel_hi:[0,0,0]
	v_mfma_scale_f32_16x16x128_f8f6f4 v[78:81], v[18:25], v[58:65], 0, v1, v198 op_sel_hi:[0,0,0]
	v_mfma_scale_f32_16x16x128_f8f6f4 v[74:77], v[26:33], v[50:57], 0, v1, v198 op_sel_hi:[0,0,0]
	v_mfma_scale_f32_16x16x128_f8f6f4 v[82:85], v[18:25], v[50:57], 0, v1, v198 op_sel_hi:[0,0,0]
	v_mfma_scale_f32_16x16x128_f8f6f4 v[86:89], v[26:33], v[42:49], 0, v1, v198 op_sel_hi:[0,0,0]
	v_mfma_scale_f32_16x16x128_f8f6f4 v[90:93], v[18:25], v[42:49], 0, v1, v198 op_sel_hi:[0,0,0]
	v_mfma_scale_f32_16x16x128_f8f6f4 v[94:97], v[26:33], v[34:41], 0, v1, v198 op_sel_hi:[0,0,0]
	v_mfma_scale_f32_16x16x128_f8f6f4 v[98:101], v[18:25], v[34:41], 0, v1, v198 op_sel_hi:[0,0,0]
	s_setprio 0
	s_setprio 1
	v_mfma_scale_f32_16x16x128_f8f6f4 v[106:109], v[10:17], v[58:65], 0, v1, v198 op_sel_hi:[0,0,0]
	v_mfma_scale_f32_16x16x128_f8f6f4 v[126:129], v[2:9], v[58:65], 0, v1, v198 op_sel_hi:[0,0,0]
	v_mfma_scale_f32_16x16x128_f8f6f4 v[114:117], v[10:17], v[50:57], 0, v1, v198 op_sel_hi:[0,0,0]
	v_mfma_scale_f32_16x16x128_f8f6f4 v[122:125], v[2:9], v[50:57], 0, v1, v198 op_sel_hi:[0,0,0]
	v_mfma_scale_f32_16x16x128_f8f6f4 v[110:113], v[10:17], v[42:49], 0, v1, v198 op_sel_hi:[0,0,0]
	v_mfma_scale_f32_16x16x128_f8f6f4 v[118:121], v[2:9], v[42:49], 0, v1, v198 op_sel_hi:[0,0,0]
	v_mfma_scale_f32_16x16x128_f8f6f4 v[102:105], v[10:17], v[34:41], 0, v1, v198 op_sel_hi:[0,0,0]
	v_mfma_scale_f32_16x16x128_f8f6f4 v[66:69], v[2:9], v[34:41], 0, v1, v198 op_sel_hi:[0,0,0]
	s_setprio 0
	s_barrier
	s_mov_b32 m0, s49
	v_lshl_add_u64 v[196:197], s[42:43], 0, v[178:179]
	ds_read_b128 v[58:61], v204 offset:16384
	ds_read_b128 v[62:65], v204 offset:17408
	ds_read_b128 v[50:53], v204 offset:18432
	ds_read_b128 v[54:57], v204 offset:19456
	ds_read_b128 v[42:45], v204 offset:20480
	ds_read_b128 v[46:49], v204 offset:21504
	ds_read_b128 v[34:37], v204 offset:22528
	ds_read_b128 v[38:41], v204 offset:23552
	global_load_lds_dwordx4 v[196:197], off
	v_lshl_add_u64 v[194:195], s[42:43], 0, v[174:175]
	s_mov_b32 m0, s50
	v_lshl_add_u64 v[192:193], s[42:43], 0, v[180:181]
	global_load_lds_dwordx4 v[194:195], off
	s_mov_b32 m0, s51
	v_lshl_add_u64 v[190:191], s[42:43], 0, v[176:177]
	global_load_lds_dwordx4 v[192:193], off
	s_mov_b32 m0, s58
	v_lshl_add_u64 v[186:187], s[38:39], 0, v[178:179]
	global_load_lds_dwordx4 v[190:191], off
	s_mov_b32 m0, s23
	v_lshl_add_u64 v[188:189], s[38:39], 0, v[174:175]
	global_load_lds_dwordx4 v[186:187], off
	s_mov_b32 m0, s59
	s_and_b64 vcc, exec, s[40:41]
	global_load_lds_dwordx4 v[188:189], off
	s_cbranch_vccz .LBB0_693
	s_waitcnt vmcnt(24)
	s_cbranch_execnz .LBB0_683

.LBB0_683:
	s_waitcnt lgkmcnt(0)
	s_barrier
	s_setprio 1
	s_mov_b32 s6, s4
	s_mov_b32 s7, s4
	s_mov_b32 s5, s4
	s_waitcnt lgkmcnt(0)
	v_mfma_scale_f32_16x16x128_f8f6f4 v[134:137], v[26:33], v[58:65], 0, v1, v198 op_sel_hi:[0,0,0]
	v_mfma_scale_f32_16x16x128_f8f6f4 v[138:141], v[18:25], v[58:65], 0, v1, v198 op_sel_hi:[0,0,0]
	v_mfma_scale_f32_16x16x128_f8f6f4 v[142:145], v[26:33], v[50:57], 0, v1, v198 op_sel_hi:[0,0,0]
	v_mfma_scale_f32_16x16x128_f8f6f4 v[146:149], v[18:25], v[50:57], 0, v1, v198 op_sel_hi:[0,0,0]
	v_mfma_scale_f32_16x16x128_f8f6f4 v[150:153], v[26:33], v[42:49], 0, v1, v198 op_sel_hi:[0,0,0]
	v_mfma_scale_f32_16x16x128_f8f6f4 v[154:157], v[18:25], v[42:49], 0, v1, v198 op_sel_hi:[0,0,0]
	v_mfma_scale_f32_16x16x128_f8f6f4 v[158:161], v[26:33], v[34:41], 0, v1, v198 op_sel_hi:[0,0,0]
	v_mfma_scale_f32_16x16x128_f8f6f4 v[162:165], v[18:25], v[34:41], 0, v1, v198 op_sel_hi:[0,0,0]
	s_setprio 0
	s_setprio 1
	v_mfma_scale_f32_16x16x128_f8f6f4 v[166:169], v[10:17], v[58:65], 0, v1, v198 op_sel_hi:[0,0,0]
	v_mfma_scale_f32_16x16x128_f8f6f4 v[170:173], v[2:9], v[58:65], 0, v1, v198 op_sel_hi:[0,0,0]
	v_mfma_scale_f32_16x16x128_f8f6f4 v[58:61], v[10:17], v[50:57], 0, v1, v198 op_sel_hi:[0,0,0]
	v_mfma_scale_f32_16x16x128_f8f6f4 v[62:65], v[2:9], v[50:57], 0, v1, v198 op_sel_hi:[0,0,0]
	v_mfma_scale_f32_16x16x128_f8f6f4 v[50:53], v[10:17], v[42:49], 0, v1, v198 op_sel_hi:[0,0,0]
	v_mfma_scale_f32_16x16x128_f8f6f4 v[54:57], v[2:9], v[42:49], 0, v1, v198 op_sel_hi:[0,0,0]
	v_mfma_scale_f32_16x16x128_f8f6f4 v[42:45], v[10:17], v[34:41], 0, v1, v198 op_sel_hi:[0,0,0]
	v_mfma_scale_f32_16x16x128_f8f6f4 v[130:133], v[2:9], v[34:41], 0, v1, v198 op_sel_hi:[0,0,0]
	s_setprio 0
	s_barrier
	s_add_i32 s5, 0, 0x18000
	s_add_i32 s6, 0, 0x1c000
	v_add_u32_e32 v205, s5, v200
	v_add_u32_e32 v206, s6, v200
	ds_read_b128 v[26:29], v205
	ds_read_b128 v[30:33], v205 offset:1024
	ds_read_b128 v[18:21], v205 offset:2048
	ds_read_b128 v[22:25], v205 offset:3072
	ds_read_b128 v[10:13], v206
	ds_read_b128 v[14:17], v206 offset:1024
	ds_read_b128 v[2:5], v206 offset:2048
	ds_read_b128 v[6:9], v206 offset:3072
	s_mov_b32 m0, s60
	v_lshl_add_u64 v[46:47], s[38:39], 0, v[180:181]
	ds_read_b128 v[34:37], v204 offset:32768
	ds_read_b128 v[38:41], v204 offset:33792
	ds_read_b128 v[208:211], v204 offset:34816
	ds_read_b128 v[212:215], v204 offset:35840
	ds_read_b128 v[216:219], v204 offset:36864
	ds_read_b128 v[220:223], v204 offset:37888
	ds_read_b128 v[224:227], v204 offset:38912
	ds_read_b128 v[228:231], v204 offset:39936
	global_load_lds_dwordx4 v[46:47], off
	v_lshl_add_u64 v[46:47], s[38:39], 0, v[176:177]
	s_mov_b32 m0, s61
	s_nop 0
	global_load_lds_dwordx4 v[46:47], off
	s_waitcnt vmcnt(8)
	s_waitcnt lgkmcnt(0)
	s_barrier
	s_setprio 1
	s_waitcnt lgkmcnt(0)
	v_mfma_scale_f32_16x16x128_f8f6f4 v[70:73], v[26:33], v[34:41], v[70:73], v1, v198 op_sel_hi:[0,0,0]
	v_mfma_scale_f32_16x16x128_f8f6f4 v[78:81], v[18:25], v[34:41], v[78:81], v1, v198 op_sel_hi:[0,0,0]
	v_mfma_scale_f32_16x16x128_f8f6f4 v[74:77], v[26:33], v[208:215], v[74:77], v1, v198 op_sel_hi:[0,0,0]
	v_mfma_scale_f32_16x16x128_f8f6f4 v[82:85], v[18:25], v[208:215], v[82:85], v1, v198 op_sel_hi:[0,0,0]
	v_mfma_scale_f32_16x16x128_f8f6f4 v[86:89], v[26:33], v[216:223], v[86:89], v1, v198 op_sel_hi:[0,0,0]
	v_mfma_scale_f32_16x16x128_f8f6f4 v[90:93], v[18:25], v[216:223], v[90:93], v1, v198 op_sel_hi:[0,0,0]
	v_mfma_scale_f32_16x16x128_f8f6f4 v[94:97], v[26:33], v[224:231], v[94:97], v1, v198 op_sel_hi:[0,0,0]
	v_mfma_scale_f32_16x16x128_f8f6f4 v[98:101], v[18:25], v[224:231], v[98:101], v1, v198 op_sel_hi:[0,0,0]
	s_setprio 0
	s_setprio 1
	v_mfma_scale_f32_16x16x128_f8f6f4 v[106:109], v[10:17], v[34:41], v[106:109], v1, v198 op_sel_hi:[0,0,0]
	v_mfma_scale_f32_16x16x128_f8f6f4 v[126:129], v[2:9], v[34:41], v[126:129], v1, v198 op_sel_hi:[0,0,0]
	v_mfma_scale_f32_16x16x128_f8f6f4 v[114:117], v[10:17], v[208:215], v[114:117], v1, v198 op_sel_hi:[0,0,0]
	v_mfma_scale_f32_16x16x128_f8f6f4 v[122:125], v[2:9], v[208:215], v[122:125], v1, v198 op_sel_hi:[0,0,0]
	v_mfma_scale_f32_16x16x128_f8f6f4 v[110:113], v[10:17], v[216:223], v[110:113], v1, v198 op_sel_hi:[0,0,0]
	v_mfma_scale_f32_16x16x128_f8f6f4 v[118:121], v[2:9], v[216:223], v[118:121], v1, v198 op_sel_hi:[0,0,0]
	v_mfma_scale_f32_16x16x128_f8f6f4 v[102:105], v[10:17], v[224:231], v[102:105], v1, v198 op_sel_hi:[0,0,0]
	v_mfma_scale_f32_16x16x128_f8f6f4 v[66:69], v[2:9], v[224:231], v[66:69], v1, v198 op_sel_hi:[0,0,0]
	s_setprio 0
	s_barrier
	s_add_i32 s5, s5, s48
	v_lshl_add_u64 v[46:47], v[196:197], 0, s[12:13]
	s_mov_b32 m0, s5
	s_add_i32 s27, s5, 0x2000
	ds_read_b128 v[34:37], v204 offset:49152
	ds_read_b128 v[38:41], v204 offset:50176
	ds_read_b128 v[208:211], v204 offset:51200
	ds_read_b128 v[212:215], v204 offset:52224
	ds_read_b128 v[216:219], v204 offset:53248
	ds_read_b128 v[220:223], v204 offset:54272
	ds_read_b128 v[224:227], v204 offset:55296
	ds_read_b128 v[228:231], v204 offset:56320
	global_load_lds_dwordx4 v[46:47], off
	v_lshl_add_u64 v[46:47], v[194:195], 0, s[12:13]
	s_mov_b32 m0, s27
	s_add_i32 s38, s6, s48
	global_load_lds_dwordx4 v[46:47], off
	v_lshl_add_u64 v[46:47], v[192:193], 0, s[12:13]
	s_mov_b32 m0, s38
	s_add_i32 s39, s38, 0x2000
	global_load_lds_dwordx4 v[46:47], off
	v_lshl_add_u64 v[46:47], v[190:191], 0, s[12:13]
	s_mov_b32 m0, s39
	s_nop 0
	global_load_lds_dwordx4 v[46:47], off
	v_lshl_add_u64 v[46:47], v[186:187], 0, s[12:13]
	s_mov_b32 m0, s62
	s_nop 0
	global_load_lds_dwordx4 v[46:47], off
	v_lshl_add_u64 v[46:47], v[188:189], 0, s[12:13]
	s_mov_b32 m0, s63
	s_nop 0
	global_load_lds_dwordx4 v[46:47], off
	s_waitcnt vmcnt(8)
	s_waitcnt lgkmcnt(0)
	s_barrier
	s_setprio 1
	s_waitcnt lgkmcnt(0)
	v_mfma_scale_f32_16x16x128_f8f6f4 v[134:137], v[26:33], v[34:41], v[134:137], v1, v198 op_sel_hi:[0,0,0]
	v_mfma_scale_f32_16x16x128_f8f6f4 v[138:141], v[18:25], v[34:41], v[138:141], v1, v198 op_sel_hi:[0,0,0]
	v_mfma_scale_f32_16x16x128_f8f6f4 v[142:145], v[26:33], v[208:215], v[142:145], v1, v198 op_sel_hi:[0,0,0]
	v_mfma_scale_f32_16x16x128_f8f6f4 v[146:149], v[18:25], v[208:215], v[146:149], v1, v198 op_sel_hi:[0,0,0]
	v_mfma_scale_f32_16x16x128_f8f6f4 v[150:153], v[26:33], v[216:223], v[150:153], v1, v198 op_sel_hi:[0,0,0]
	v_mfma_scale_f32_16x16x128_f8f6f4 v[154:157], v[18:25], v[216:223], v[154:157], v1, v198 op_sel_hi:[0,0,0]
	v_mfma_scale_f32_16x16x128_f8f6f4 v[158:161], v[26:33], v[224:231], v[158:161], v1, v198 op_sel_hi:[0,0,0]
	v_mfma_scale_f32_16x16x128_f8f6f4 v[162:165], v[18:25], v[224:231], v[162:165], v1, v198 op_sel_hi:[0,0,0]
	s_setprio 0
	s_setprio 1
	v_mfma_scale_f32_16x16x128_f8f6f4 v[166:169], v[10:17], v[34:41], v[166:169], v1, v198 op_sel_hi:[0,0,0]
	v_mfma_scale_f32_16x16x128_f8f6f4 v[170:173], v[2:9], v[34:41], v[170:173], v1, v198 op_sel_hi:[0,0,0]
	v_mfma_scale_f32_16x16x128_f8f6f4 v[58:61], v[10:17], v[208:215], v[58:61], v1, v198 op_sel_hi:[0,0,0]
	v_mfma_scale_f32_16x16x128_f8f6f4 v[62:65], v[2:9], v[208:215], v[62:65], v1, v198 op_sel_hi:[0,0,0]
	v_mfma_scale_f32_16x16x128_f8f6f4 v[50:53], v[10:17], v[216:223], v[50:53], v1, v198 op_sel_hi:[0,0,0]
	v_mfma_scale_f32_16x16x128_f8f6f4 v[54:57], v[2:9], v[216:223], v[54:57], v1, v198 op_sel_hi:[0,0,0]
	v_mfma_scale_f32_16x16x128_f8f6f4 v[42:45], v[10:17], v[224:231], v[42:45], v1, v198 op_sel_hi:[0,0,0]
	v_mfma_scale_f32_16x16x128_f8f6f4 v[130:133], v[2:9], v[224:231], v[130:133], v1, v198 op_sel_hi:[0,0,0]
	s_setprio 0
	s_barrier
	s_andn2_b64 vcc, exec, s[20:21]
	s_cbranch_vccnz .LBB0_686
	s_add_u32 s6, s34, 0x180
	s_addc_u32 s7, s35, 0
	s_add_u32 s40, s36, 0x200
	s_addc_u32 s41, s37, 0
	s_mov_b32 s42, 4

.LBB0_883:
	s_and_b64 s[4:5], s[54:55], exec
	s_cselect_b32 s31, s79, s79
	s_cselect_b32 s34, s78, s78
	s_cselect_b32 s35, s1, s95
	s_cselect_b32 s39, s0, s94
	s_add_u32 s16, s78, 0x100
	s_addc_u32 s17, s79, 0
	s_and_b64 s[4:5], s[88:89], exec
	s_cselect_b32 s5, s31, s17
	s_cselect_b32 s4, s34, s16
	s_add_u32 s49, s94, 0x100
	s_waitcnt lgkmcnt(0)
	s_addc_u32 s50, s95, 0
	s_and_b64 s[16:17], s[88:89], exec
	s_cselect_b32 vcc_hi, s35, s50
	s_cselect_b32 vcc_lo, s39, s49
	s_barrier
	s_setprio 1
	s_mov_b32 s50, s48
	s_mov_b32 s51, s48
	s_mov_b32 s49, s48
	s_waitcnt lgkmcnt(0)
	v_mfma_scale_f32_16x16x128_f8f6f4 v[162:165], v[26:33], v[58:65], 0, v1, v206 op_sel_hi:[0,0,0]
	v_mfma_scale_f32_16x16x128_f8f6f4 v[158:161], v[18:25], v[58:65], 0, v1, v206 op_sel_hi:[0,0,0]
	v_mfma_scale_f32_16x16x128_f8f6f4 v[146:149], v[26:33], v[50:57], 0, v1, v206 op_sel_hi:[0,0,0]
	v_mfma_scale_f32_16x16x128_f8f6f4 v[142:145], v[18:25], v[50:57], 0, v1, v206 op_sel_hi:[0,0,0]
	v_mfma_scale_f32_16x16x128_f8f6f4 v[130:133], v[26:33], v[42:49], 0, v1, v206 op_sel_hi:[0,0,0]
	v_mfma_scale_f32_16x16x128_f8f6f4 v[126:129], v[18:25], v[42:49], 0, v1, v206 op_sel_hi:[0,0,0]
	v_mfma_scale_f32_16x16x128_f8f6f4 v[110:113], v[26:33], v[34:41], 0, v1, v206 op_sel_hi:[0,0,0]
	v_mfma_scale_f32_16x16x128_f8f6f4 v[106:109], v[18:25], v[34:41], 0, v1, v206 op_sel_hi:[0,0,0]
	s_setprio 0
	s_setprio 1
	v_mfma_scale_f32_16x16x128_f8f6f4 v[170:173], v[10:17], v[58:65], 0, v1, v206 op_sel_hi:[0,0,0]
	v_mfma_scale_f32_16x16x128_f8f6f4 v[166:169], v[2:9], v[58:65], 0, v1, v206 op_sel_hi:[0,0,0]
	v_mfma_scale_f32_16x16x128_f8f6f4 v[154:157], v[10:17], v[50:57], 0, v1, v206 op_sel_hi:[0,0,0]
	v_mfma_scale_f32_16x16x128_f8f6f4 v[150:153], v[2:9], v[50:57], 0, v1, v206 op_sel_hi:[0,0,0]
	v_mfma_scale_f32_16x16x128_f8f6f4 v[138:141], v[10:17], v[42:49], 0, v1, v206 op_sel_hi:[0,0,0]
	v_mfma_scale_f32_16x16x128_f8f6f4 v[134:137], v[2:9], v[42:49], 0, v1, v206 op_sel_hi:[0,0,0]
	v_mfma_scale_f32_16x16x128_f8f6f4 v[122:125], v[10:17], v[34:41], 0, v1, v206 op_sel_hi:[0,0,0]
	v_mfma_scale_f32_16x16x128_f8f6f4 v[102:105], v[2:9], v[34:41], 0, v1, v206 op_sel_hi:[0,0,0]
	s_setprio 0
	s_barrier
	s_mov_b32 m0, s8
	v_lshl_add_u64 v[200:201], vcc, 0, v[174:175]
	ds_read_b128 v[58:61], v215 offset:16384
	ds_read_b128 v[62:65], v215 offset:17408
	ds_read_b128 v[50:53], v215 offset:18432
	ds_read_b128 v[54:57], v215 offset:19456
	ds_read_b128 v[42:45], v215 offset:20480
	ds_read_b128 v[46:49], v215 offset:21504
	ds_read_b128 v[34:37], v215 offset:22528
	ds_read_b128 v[38:41], v215 offset:23552
	global_load_lds_dwordx4 v[200:201], off
	v_lshl_add_u64 v[198:199], vcc, 0, v[178:179]
	s_mov_b32 m0, s9
	v_lshl_add_u64 v[196:197], vcc, 0, v[176:177]
	global_load_lds_dwordx4 v[198:199], off
	s_mov_b32 m0, s18
	v_lshl_add_u64 v[194:195], vcc, 0, v[180:181]
	global_load_lds_dwordx4 v[196:197], off
	s_mov_b32 m0, s19
	s_and_b64 vcc, exec, s[6:7]
	global_load_lds_dwordx4 v[194:195], off
	s_mov_b32 m0, s15
	s_nop 0
	global_load_lds_dwordx4 v190, s[4:5]
	s_mov_b32 m0, s20
	s_nop 0
	global_load_lds_dwordx4 v192, s[4:5]
	s_cbranch_vccz .LBB0_890
	s_waitcnt vmcnt(16)
	s_cbranch_execnz .LBB0_886

.LBB0_886:
	s_waitcnt lgkmcnt(0)
	v_mov_b32_e32 v193, v191
	v_lshl_add_u64 v[202:203], s[4:5], 0, v[190:191]
	v_lshl_add_u64 v[204:205], s[4:5], 0, v[192:193]
	s_barrier
	s_setprio 1
	s_mov_b32 s50, s48
	s_mov_b32 s51, s48
	s_mov_b32 s49, s48
	s_waitcnt lgkmcnt(0)
	v_mfma_scale_f32_16x16x128_f8f6f4 v[98:101], v[26:33], v[58:65], 0, v1, v206 op_sel_hi:[0,0,0]
	v_mfma_scale_f32_16x16x128_f8f6f4 v[94:97], v[18:25], v[58:65], 0, v1, v206 op_sel_hi:[0,0,0]
	v_mfma_scale_f32_16x16x128_f8f6f4 v[90:93], v[26:33], v[50:57], 0, v1, v206 op_sel_hi:[0,0,0]
	v_mfma_scale_f32_16x16x128_f8f6f4 v[86:89], v[18:25], v[50:57], 0, v1, v206 op_sel_hi:[0,0,0]
	v_mfma_scale_f32_16x16x128_f8f6f4 v[82:85], v[26:33], v[42:49], 0, v1, v206 op_sel_hi:[0,0,0]
	v_mfma_scale_f32_16x16x128_f8f6f4 v[78:81], v[18:25], v[42:49], 0, v1, v206 op_sel_hi:[0,0,0]
	v_mfma_scale_f32_16x16x128_f8f6f4 v[74:77], v[26:33], v[34:41], 0, v1, v206 op_sel_hi:[0,0,0]
	v_mfma_scale_f32_16x16x128_f8f6f4 v[70:73], v[18:25], v[34:41], 0, v1, v206 op_sel_hi:[0,0,0]
	s_setprio 0
	s_setprio 1
	v_mfma_scale_f32_16x16x128_f8f6f4 v[118:121], v[10:17], v[58:65], 0, v1, v206 op_sel_hi:[0,0,0]
	v_mfma_scale_f32_16x16x128_f8f6f4 v[114:117], v[2:9], v[58:65], 0, v1, v206 op_sel_hi:[0,0,0]
	v_mfma_scale_f32_16x16x128_f8f6f4 v[62:65], v[10:17], v[50:57], 0, v1, v206 op_sel_hi:[0,0,0]
	v_mfma_scale_f32_16x16x128_f8f6f4 v[58:61], v[2:9], v[50:57], 0, v1, v206 op_sel_hi:[0,0,0]
	v_mfma_scale_f32_16x16x128_f8f6f4 v[54:57], v[10:17], v[42:49], 0, v1, v206 op_sel_hi:[0,0,0]
	v_mfma_scale_f32_16x16x128_f8f6f4 v[50:53], v[2:9], v[42:49], 0, v1, v206 op_sel_hi:[0,0,0]
	v_mfma_scale_f32_16x16x128_f8f6f4 v[42:45], v[10:17], v[34:41], 0, v1, v206 op_sel_hi:[0,0,0]
	v_mfma_scale_f32_16x16x128_f8f6f4 v[66:69], v[2:9], v[34:41], 0, v1, v206 op_sel_hi:[0,0,0]
	s_setprio 0
	s_barrier
	s_add_i32 s16, 0, 0x18000
	s_add_i32 s49, 0, 0x1c000
	v_add_u32_e32 v187, s16, v185
	v_add_u32_e32 v189, s49, v185
	ds_read_b128 v[26:29], v187
	ds_read_b128 v[30:33], v187 offset:1024
	ds_read_b128 v[18:21], v187 offset:2048
	ds_read_b128 v[22:25], v187 offset:3072
	ds_read_b128 v[10:13], v189
	ds_read_b128 v[14:17], v189 offset:1024
	ds_read_b128 v[2:5], v189 offset:2048
	ds_read_b128 v[6:9], v189 offset:3072
	s_mov_b32 m0, s21
	ds_read_b128 v[34:37], v215 offset:32768
	ds_read_b128 v[38:41], v215 offset:33792
	ds_read_b128 v[222:225], v215 offset:34816
	ds_read_b128 v[226:229], v215 offset:35840
	ds_read_b128 v[230:233], v215 offset:36864
	ds_read_b128 v[234:237], v215 offset:37888
	ds_read_b128 v[238:241], v215 offset:38912
	ds_read_b128 v[242:245], v215 offset:39936
	global_load_lds_dwordx4 v220, s[4:5]
	s_mov_b32 m0, s22
	s_nop 0
	global_load_lds_dwordx4 v219, s[4:5]
	s_waitcnt vmcnt(8)
	s_waitcnt lgkmcnt(0)
	s_barrier
	s_setprio 1
	s_waitcnt lgkmcnt(0)
	v_mfma_scale_f32_16x16x128_f8f6f4 v[162:165], v[26:33], v[34:41], v[162:165], v1, v206 op_sel_hi:[0,0,0]
	v_mfma_scale_f32_16x16x128_f8f6f4 v[158:161], v[18:25], v[34:41], v[158:161], v1, v206 op_sel_hi:[0,0,0]
	v_mfma_scale_f32_16x16x128_f8f6f4 v[146:149], v[26:33], v[222:229], v[146:149], v1, v206 op_sel_hi:[0,0,0]
	v_mfma_scale_f32_16x16x128_f8f6f4 v[142:145], v[18:25], v[222:229], v[142:145], v1, v206 op_sel_hi:[0,0,0]
	v_mfma_scale_f32_16x16x128_f8f6f4 v[130:133], v[26:33], v[230:237], v[130:133], v1, v206 op_sel_hi:[0,0,0]
	v_mfma_scale_f32_16x16x128_f8f6f4 v[126:129], v[18:25], v[230:237], v[126:129], v1, v206 op_sel_hi:[0,0,0]
	v_mfma_scale_f32_16x16x128_f8f6f4 v[110:113], v[26:33], v[238:245], v[110:113], v1, v206 op_sel_hi:[0,0,0]
	v_mfma_scale_f32_16x16x128_f8f6f4 v[106:109], v[18:25], v[238:245], v[106:109], v1, v206 op_sel_hi:[0,0,0]
	s_setprio 0
	s_setprio 1
	v_mfma_scale_f32_16x16x128_f8f6f4 v[170:173], v[10:17], v[34:41], v[170:173], v1, v206 op_sel_hi:[0,0,0]
	v_mfma_scale_f32_16x16x128_f8f6f4 v[166:169], v[2:9], v[34:41], v[166:169], v1, v206 op_sel_hi:[0,0,0]
	v_mfma_scale_f32_16x16x128_f8f6f4 v[154:157], v[10:17], v[222:229], v[154:157], v1, v206 op_sel_hi:[0,0,0]
	v_mfma_scale_f32_16x16x128_f8f6f4 v[150:153], v[2:9], v[222:229], v[150:153], v1, v206 op_sel_hi:[0,0,0]
	v_mfma_scale_f32_16x16x128_f8f6f4 v[138:141], v[10:17], v[230:237], v[138:141], v1, v206 op_sel_hi:[0,0,0]
	v_mfma_scale_f32_16x16x128_f8f6f4 v[134:137], v[2:9], v[230:237], v[134:137], v1, v206 op_sel_hi:[0,0,0]
	v_mfma_scale_f32_16x16x128_f8f6f4 v[122:125], v[10:17], v[238:245], v[122:125], v1, v206 op_sel_hi:[0,0,0]
	v_mfma_scale_f32_16x16x128_f8f6f4 v[102:105], v[2:9], v[238:245], v[102:105], v1, v206 op_sel_hi:[0,0,0]
	s_setprio 0
	s_barrier
	s_add_i32 s16, s16, s13
	v_lshl_add_u64 v[46:47], v[200:201], 0, s[82:83]
	s_mov_b32 m0, s16
	s_add_i32 s17, s16, 0x2000
	ds_read_b128 v[34:37], v215 offset:49152
	ds_read_b128 v[38:41], v215 offset:50176
	ds_read_b128 v[222:225], v215 offset:51200
	ds_read_b128 v[226:229], v215 offset:52224
	ds_read_b128 v[230:233], v215 offset:53248
	ds_read_b128 v[234:237], v215 offset:54272
	ds_read_b128 v[238:241], v215 offset:55296
	ds_read_b128 v[242:245], v215 offset:56320
	global_load_lds_dwordx4 v[46:47], off
	v_lshl_add_u64 v[46:47], v[198:199], 0, s[82:83]
	s_mov_b32 m0, s17
	s_add_i32 s49, s49, s13
	global_load_lds_dwordx4 v[46:47], off
	v_lshl_add_u64 v[46:47], v[196:197], 0, s[82:83]
	s_mov_b32 m0, s49
	s_add_i32 s65, s49, 0x2000
	global_load_lds_dwordx4 v[46:47], off
	v_lshl_add_u64 v[46:47], v[194:195], 0, s[82:83]
	s_mov_b32 m0, s65
	s_nop 0
	global_load_lds_dwordx4 v[46:47], off
	v_lshl_add_u64 v[46:47], v[202:203], 0, s[82:83]
	s_mov_b32 m0, s23
	s_nop 0
	global_load_lds_dwordx4 v[46:47], off
	v_lshl_add_u64 v[46:47], v[204:205], 0, s[82:83]
	s_mov_b32 m0, s24
	s_nop 0
	global_load_lds_dwordx4 v[46:47], off
	s_waitcnt vmcnt(8)
	s_waitcnt lgkmcnt(0)
	s_barrier
	s_setprio 1
	s_waitcnt lgkmcnt(0)
	v_mfma_scale_f32_16x16x128_f8f6f4 v[98:101], v[26:33], v[34:41], v[98:101], v1, v206 op_sel_hi:[0,0,0]
	v_mfma_scale_f32_16x16x128_f8f6f4 v[94:97], v[18:25], v[34:41], v[94:97], v1, v206 op_sel_hi:[0,0,0]
	v_mfma_scale_f32_16x16x128_f8f6f4 v[90:93], v[26:33], v[222:229], v[90:93], v1, v206 op_sel_hi:[0,0,0]
	v_mfma_scale_f32_16x16x128_f8f6f4 v[86:89], v[18:25], v[222:229], v[86:89], v1, v206 op_sel_hi:[0,0,0]
	v_mfma_scale_f32_16x16x128_f8f6f4 v[82:85], v[26:33], v[230:237], v[82:85], v1, v206 op_sel_hi:[0,0,0]
	v_mfma_scale_f32_16x16x128_f8f6f4 v[78:81], v[18:25], v[230:237], v[78:81], v1, v206 op_sel_hi:[0,0,0]
	v_mfma_scale_f32_16x16x128_f8f6f4 v[74:77], v[26:33], v[238:245], v[74:77], v1, v206 op_sel_hi:[0,0,0]
	v_mfma_scale_f32_16x16x128_f8f6f4 v[70:73], v[18:25], v[238:245], v[70:73], v1, v206 op_sel_hi:[0,0,0]
	s_setprio 0
	s_setprio 1
	v_mfma_scale_f32_16x16x128_f8f6f4 v[118:121], v[10:17], v[34:41], v[118:121], v1, v206 op_sel_hi:[0,0,0]
	v_mfma_scale_f32_16x16x128_f8f6f4 v[114:117], v[2:9], v[34:41], v[114:117], v1, v206 op_sel_hi:[0,0,0]
	v_mfma_scale_f32_16x16x128_f8f6f4 v[62:65], v[10:17], v[222:229], v[62:65], v1, v206 op_sel_hi:[0,0,0]
	v_mfma_scale_f32_16x16x128_f8f6f4 v[58:61], v[2:9], v[222:229], v[58:61], v1, v206 op_sel_hi:[0,0,0]
	v_mfma_scale_f32_16x16x128_f8f6f4 v[54:57], v[10:17], v[230:237], v[54:57], v1, v206 op_sel_hi:[0,0,0]
	v_mfma_scale_f32_16x16x128_f8f6f4 v[50:53], v[2:9], v[230:237], v[50:53], v1, v206 op_sel_hi:[0,0,0]
	v_mfma_scale_f32_16x16x128_f8f6f4 v[42:45], v[10:17], v[238:245], v[42:45], v1, v206 op_sel_hi:[0,0,0]
	v_mfma_scale_f32_16x16x128_f8f6f4 v[66:69], v[2:9], v[238:245], v[66:69], v1, v206 op_sel_hi:[0,0,0]
	s_setprio 0
	s_barrier
	s_andn2_b64 vcc, exec, s[88:89]
	s_cbranch_vccz .LBB0_891
	s_andn2_b64 vcc, exec, s[90:91]
	s_cbranch_vccz .LBB0_892
	s_branch .LBB0_899

.LBB0_987:
	s_and_b64 s[4:5], s[92:93], exec
	s_cselect_b32 s65, s39, s1
	s_cselect_b32 s16, s38, s0
	s_cselect_b32 s17, s85, s95
	s_cselect_b32 s66, s84, s94
	s_add_u32 s49, s0, 0x100
	s_addc_u32 s50, s1, 0
	s_and_b64 s[4:5], s[80:81], exec
	s_cselect_b32 s5, s65, s50
	s_cselect_b32 s4, s16, s49
	s_add_u32 s49, s94, 0x100
	s_waitcnt lgkmcnt(0)
	s_addc_u32 s67, s95, 0
	s_and_b64 s[50:51], s[80:81], exec
	s_cselect_b32 s97, s17, s67
	s_cselect_b32 s96, s66, s49
	s_barrier
	s_setprio 1
	s_mov_b32 s50, s48
	s_mov_b32 s51, s48
	s_mov_b32 s49, s48
	s_waitcnt lgkmcnt(0)
	v_mfma_scale_f32_16x16x128_f8f6f4 v[126:129], v[26:33], v[58:65], 0, v1, v198 op_sel_hi:[0,0,0]
	v_mfma_scale_f32_16x16x128_f8f6f4 v[130:133], v[18:25], v[58:65], 0, v1, v198 op_sel_hi:[0,0,0]
	v_mfma_scale_f32_16x16x128_f8f6f4 v[114:117], v[26:33], v[50:57], 0, v1, v198 op_sel_hi:[0,0,0]
	v_mfma_scale_f32_16x16x128_f8f6f4 v[106:109], v[18:25], v[50:57], 0, v1, v198 op_sel_hi:[0,0,0]
	v_mfma_scale_f32_16x16x128_f8f6f4 v[94:97], v[26:33], v[42:49], 0, v1, v198 op_sel_hi:[0,0,0]
	v_mfma_scale_f32_16x16x128_f8f6f4 v[90:93], v[18:25], v[42:49], 0, v1, v198 op_sel_hi:[0,0,0]
	v_mfma_scale_f32_16x16x128_f8f6f4 v[78:81], v[26:33], v[34:41], 0, v1, v198 op_sel_hi:[0,0,0]
	v_mfma_scale_f32_16x16x128_f8f6f4 v[74:77], v[18:25], v[34:41], 0, v1, v198 op_sel_hi:[0,0,0]
	s_setprio 0
	s_setprio 1
	v_mfma_scale_f32_16x16x128_f8f6f4 v[158:161], v[10:17], v[58:65], 0, v1, v198 op_sel_hi:[0,0,0]
	v_mfma_scale_f32_16x16x128_f8f6f4 v[162:165], v[2:9], v[58:65], 0, v1, v198 op_sel_hi:[0,0,0]
	v_mfma_scale_f32_16x16x128_f8f6f4 v[154:157], v[10:17], v[50:57], 0, v1, v198 op_sel_hi:[0,0,0]
	v_mfma_scale_f32_16x16x128_f8f6f4 v[150:153], v[2:9], v[50:57], 0, v1, v198 op_sel_hi:[0,0,0]
	v_mfma_scale_f32_16x16x128_f8f6f4 v[138:141], v[10:17], v[42:49], 0, v1, v198 op_sel_hi:[0,0,0]
	v_mfma_scale_f32_16x16x128_f8f6f4 v[134:137], v[2:9], v[42:49], 0, v1, v198 op_sel_hi:[0,0,0]
	v_mfma_scale_f32_16x16x128_f8f6f4 v[110:113], v[10:17], v[34:41], 0, v1, v198 op_sel_hi:[0,0,0]
	v_mfma_scale_f32_16x16x128_f8f6f4 v[66:69], v[2:9], v[34:41], 0, v1, v198 op_sel_hi:[0,0,0]
	s_setprio 0
	s_barrier
	s_mov_b32 m0, s18
	v_lshl_add_u64 v[196:197], s[96:97], 0, v[174:175]
	ds_read_b128 v[58:61], v203 offset:16384
	ds_read_b128 v[62:65], v203 offset:17408
	ds_read_b128 v[50:53], v203 offset:18432
	ds_read_b128 v[54:57], v203 offset:19456
	ds_read_b128 v[42:45], v203 offset:20480
	ds_read_b128 v[46:49], v203 offset:21504
	ds_read_b128 v[34:37], v203 offset:22528
	ds_read_b128 v[38:41], v203 offset:23552
	global_load_lds_dwordx4 v[196:197], off
	v_lshl_add_u64 v[194:195], s[96:97], 0, v[178:179]
	s_mov_b32 m0, s19
	v_lshl_add_u64 v[192:193], s[96:97], 0, v[176:177]
	global_load_lds_dwordx4 v[194:195], off
	s_mov_b32 m0, s20
	v_lshl_add_u64 v[190:191], s[96:97], 0, v[180:181]
	global_load_lds_dwordx4 v[192:193], off
	s_mov_b32 m0, s21
	v_lshl_add_u64 v[186:187], s[4:5], 0, v[174:175]
	global_load_lds_dwordx4 v[190:191], off
	s_mov_b32 m0, s15
	v_lshl_add_u64 v[188:189], s[4:5], 0, v[178:179]
	global_load_lds_dwordx4 v[186:187], off
	s_mov_b32 m0, s22
	s_and_b64 vcc, exec, s[6:7]
	global_load_lds_dwordx4 v[188:189], off
	s_cbranch_vccz .LBB0_1011
	s_waitcnt vmcnt(16)
	s_cbranch_execnz .LBB0_990

.LBB0_990:
	s_waitcnt lgkmcnt(0)
	s_barrier
	s_setprio 1
	s_mov_b32 s50, s48
	s_mov_b32 s51, s48
	s_mov_b32 s49, s48
	s_waitcnt lgkmcnt(0)
	v_mfma_scale_f32_16x16x128_f8f6f4 v[146:149], v[26:33], v[58:65], 0, v1, v198 op_sel_hi:[0,0,0]
	v_mfma_scale_f32_16x16x128_f8f6f4 v[142:145], v[18:25], v[58:65], 0, v1, v198 op_sel_hi:[0,0,0]
	v_mfma_scale_f32_16x16x128_f8f6f4 v[122:125], v[26:33], v[50:57], 0, v1, v198 op_sel_hi:[0,0,0]
	v_mfma_scale_f32_16x16x128_f8f6f4 v[118:121], v[18:25], v[50:57], 0, v1, v198 op_sel_hi:[0,0,0]
	v_mfma_scale_f32_16x16x128_f8f6f4 v[102:105], v[26:33], v[42:49], 0, v1, v198 op_sel_hi:[0,0,0]
	v_mfma_scale_f32_16x16x128_f8f6f4 v[98:101], v[18:25], v[42:49], 0, v1, v198 op_sel_hi:[0,0,0]
	v_mfma_scale_f32_16x16x128_f8f6f4 v[86:89], v[26:33], v[34:41], 0, v1, v198 op_sel_hi:[0,0,0]
	v_mfma_scale_f32_16x16x128_f8f6f4 v[82:85], v[18:25], v[34:41], 0, v1, v198 op_sel_hi:[0,0,0]
	s_setprio 0
	s_setprio 1
	v_mfma_scale_f32_16x16x128_f8f6f4 v[170:173], v[10:17], v[58:65], 0, v1, v198 op_sel_hi:[0,0,0]
	v_mfma_scale_f32_16x16x128_f8f6f4 v[166:169], v[2:9], v[58:65], 0, v1, v198 op_sel_hi:[0,0,0]
	v_mfma_scale_f32_16x16x128_f8f6f4 v[62:65], v[10:17], v[50:57], 0, v1, v198 op_sel_hi:[0,0,0]
	v_mfma_scale_f32_16x16x128_f8f6f4 v[58:61], v[2:9], v[50:57], 0, v1, v198 op_sel_hi:[0,0,0]
	v_mfma_scale_f32_16x16x128_f8f6f4 v[54:57], v[10:17], v[42:49], 0, v1, v198 op_sel_hi:[0,0,0]
	v_mfma_scale_f32_16x16x128_f8f6f4 v[50:53], v[2:9], v[42:49], 0, v1, v198 op_sel_hi:[0,0,0]
	v_mfma_scale_f32_16x16x128_f8f6f4 v[42:45], v[10:17], v[34:41], 0, v1, v198 op_sel_hi:[0,0,0]
	v_mfma_scale_f32_16x16x128_f8f6f4 v[70:73], v[2:9], v[34:41], 0, v1, v198 op_sel_hi:[0,0,0]
	s_setprio 0
	s_barrier
	s_add_i32 s49, 0, 0x18000
	s_add_i32 s51, 0, 0x1c000
	v_add_u32_e32 v205, s49, v199
	v_add_u32_e32 v206, s51, v199
	ds_read_b128 v[26:29], v205
	ds_read_b128 v[30:33], v205 offset:1024
	ds_read_b128 v[18:21], v205 offset:2048
	ds_read_b128 v[22:25], v205 offset:3072
	ds_read_b128 v[10:13], v206
	ds_read_b128 v[14:17], v206 offset:1024
	ds_read_b128 v[2:5], v206 offset:2048
	ds_read_b128 v[6:9], v206 offset:3072
	s_mov_b32 m0, s23
	v_lshl_add_u64 v[46:47], s[4:5], 0, v[176:177]
	ds_read_b128 v[34:37], v203 offset:32768
	ds_read_b128 v[38:41], v203 offset:33792
	ds_read_b128 v[208:211], v203 offset:34816
	ds_read_b128 v[212:215], v203 offset:35840
	ds_read_b128 v[216:219], v203 offset:36864
	ds_read_b128 v[220:223], v203 offset:37888
	ds_read_b128 v[224:227], v203 offset:38912
	ds_read_b128 v[228:231], v203 offset:39936
	global_load_lds_dwordx4 v[46:47], off
	v_lshl_add_u64 v[46:47], s[4:5], 0, v[180:181]
	s_mov_b32 m0, s24
	s_nop 0
	global_load_lds_dwordx4 v[46:47], off
	s_waitcnt vmcnt(8)
	s_waitcnt lgkmcnt(0)
	s_barrier
	s_setprio 1
	s_waitcnt lgkmcnt(0)
	v_mfma_scale_f32_16x16x128_f8f6f4 v[126:129], v[26:33], v[34:41], v[126:129], v1, v198 op_sel_hi:[0,0,0]
	v_mfma_scale_f32_16x16x128_f8f6f4 v[130:133], v[18:25], v[34:41], v[130:133], v1, v198 op_sel_hi:[0,0,0]
	v_mfma_scale_f32_16x16x128_f8f6f4 v[114:117], v[26:33], v[208:215], v[114:117], v1, v198 op_sel_hi:[0,0,0]
	v_mfma_scale_f32_16x16x128_f8f6f4 v[106:109], v[18:25], v[208:215], v[106:109], v1, v198 op_sel_hi:[0,0,0]
	v_mfma_scale_f32_16x16x128_f8f6f4 v[94:97], v[26:33], v[216:223], v[94:97], v1, v198 op_sel_hi:[0,0,0]
	v_mfma_scale_f32_16x16x128_f8f6f4 v[90:93], v[18:25], v[216:223], v[90:93], v1, v198 op_sel_hi:[0,0,0]
	v_mfma_scale_f32_16x16x128_f8f6f4 v[78:81], v[26:33], v[224:231], v[78:81], v1, v198 op_sel_hi:[0,0,0]
	v_mfma_scale_f32_16x16x128_f8f6f4 v[74:77], v[18:25], v[224:231], v[74:77], v1, v198 op_sel_hi:[0,0,0]
	s_setprio 0
	s_setprio 1
	v_mfma_scale_f32_16x16x128_f8f6f4 v[158:161], v[10:17], v[34:41], v[158:161], v1, v198 op_sel_hi:[0,0,0]
	v_mfma_scale_f32_16x16x128_f8f6f4 v[162:165], v[2:9], v[34:41], v[162:165], v1, v198 op_sel_hi:[0,0,0]
	v_mfma_scale_f32_16x16x128_f8f6f4 v[154:157], v[10:17], v[208:215], v[154:157], v1, v198 op_sel_hi:[0,0,0]
	v_mfma_scale_f32_16x16x128_f8f6f4 v[150:153], v[2:9], v[208:215], v[150:153], v1, v198 op_sel_hi:[0,0,0]
	v_mfma_scale_f32_16x16x128_f8f6f4 v[138:141], v[10:17], v[216:223], v[138:141], v1, v198 op_sel_hi:[0,0,0]
	v_mfma_scale_f32_16x16x128_f8f6f4 v[134:137], v[2:9], v[216:223], v[134:137], v1, v198 op_sel_hi:[0,0,0]
	v_mfma_scale_f32_16x16x128_f8f6f4 v[110:113], v[10:17], v[224:231], v[110:113], v1, v198 op_sel_hi:[0,0,0]
	v_mfma_scale_f32_16x16x128_f8f6f4 v[66:69], v[2:9], v[224:231], v[66:69], v1, v198 op_sel_hi:[0,0,0]
	s_setprio 0
	s_barrier
	s_add_i32 s49, s49, s14
	v_lshl_add_u64 v[46:47], v[196:197], 0, s[54:55]
	s_mov_b32 m0, s49
	s_add_i32 s50, s49, 0x2000
	ds_read_b128 v[34:37], v203 offset:49152
	ds_read_b128 v[38:41], v203 offset:50176
	ds_read_b128 v[208:211], v203 offset:51200
	ds_read_b128 v[212:215], v203 offset:52224
	ds_read_b128 v[216:219], v203 offset:53248
	ds_read_b128 v[220:223], v203 offset:54272
	ds_read_b128 v[224:227], v203 offset:55296
	ds_read_b128 v[228:231], v203 offset:56320
	global_load_lds_dwordx4 v[46:47], off
	v_lshl_add_u64 v[46:47], v[194:195], 0, s[54:55]
	s_mov_b32 m0, s50
	s_add_i32 s51, s51, s14
	global_load_lds_dwordx4 v[46:47], off
	v_lshl_add_u64 v[46:47], v[192:193], 0, s[54:55]
	s_mov_b32 m0, s51
	s_add_i32 s67, s51, 0x2000
	global_load_lds_dwordx4 v[46:47], off
	v_lshl_add_u64 v[46:47], v[190:191], 0, s[54:55]
	s_mov_b32 m0, s67
	s_nop 0
	global_load_lds_dwordx4 v[46:47], off
	v_lshl_add_u64 v[46:47], v[186:187], 0, s[54:55]
	s_mov_b32 m0, s26
	s_nop 0
	global_load_lds_dwordx4 v[46:47], off
	v_lshl_add_u64 v[46:47], v[188:189], 0, s[54:55]
	s_mov_b32 m0, s27
	s_nop 0
	global_load_lds_dwordx4 v[46:47], off
	s_waitcnt vmcnt(8)
	s_waitcnt lgkmcnt(0)
	s_barrier
	s_setprio 1
	s_waitcnt lgkmcnt(0)
	v_mfma_scale_f32_16x16x128_f8f6f4 v[146:149], v[26:33], v[34:41], v[146:149], v1, v198 op_sel_hi:[0,0,0]
	v_mfma_scale_f32_16x16x128_f8f6f4 v[142:145], v[18:25], v[34:41], v[142:145], v1, v198 op_sel_hi:[0,0,0]
	v_mfma_scale_f32_16x16x128_f8f6f4 v[122:125], v[26:33], v[208:215], v[122:125], v1, v198 op_sel_hi:[0,0,0]
	v_mfma_scale_f32_16x16x128_f8f6f4 v[118:121], v[18:25], v[208:215], v[118:121], v1, v198 op_sel_hi:[0,0,0]
	v_mfma_scale_f32_16x16x128_f8f6f4 v[102:105], v[26:33], v[216:223], v[102:105], v1, v198 op_sel_hi:[0,0,0]
	v_mfma_scale_f32_16x16x128_f8f6f4 v[98:101], v[18:25], v[216:223], v[98:101], v1, v198 op_sel_hi:[0,0,0]
	v_mfma_scale_f32_16x16x128_f8f6f4 v[86:89], v[26:33], v[224:231], v[86:89], v1, v198 op_sel_hi:[0,0,0]
	v_mfma_scale_f32_16x16x128_f8f6f4 v[82:85], v[18:25], v[224:231], v[82:85], v1, v198 op_sel_hi:[0,0,0]
	s_setprio 0
	s_setprio 1
	v_mfma_scale_f32_16x16x128_f8f6f4 v[170:173], v[10:17], v[34:41], v[170:173], v1, v198 op_sel_hi:[0,0,0]
	v_mfma_scale_f32_16x16x128_f8f6f4 v[166:169], v[2:9], v[34:41], v[166:169], v1, v198 op_sel_hi:[0,0,0]
	v_mfma_scale_f32_16x16x128_f8f6f4 v[62:65], v[10:17], v[208:215], v[62:65], v1, v198 op_sel_hi:[0,0,0]
	v_mfma_scale_f32_16x16x128_f8f6f4 v[58:61], v[2:9], v[208:215], v[58:61], v1, v198 op_sel_hi:[0,0,0]
	v_mfma_scale_f32_16x16x128_f8f6f4 v[54:57], v[10:17], v[216:223], v[54:57], v1, v198 op_sel_hi:[0,0,0]
	v_mfma_scale_f32_16x16x128_f8f6f4 v[50:53], v[2:9], v[216:223], v[50:53], v1, v198 op_sel_hi:[0,0,0]
	v_mfma_scale_f32_16x16x128_f8f6f4 v[42:45], v[10:17], v[224:231], v[42:45], v1, v198 op_sel_hi:[0,0,0]
	v_mfma_scale_f32_16x16x128_f8f6f4 v[70:73], v[2:9], v[224:231], v[70:73], v1, v198 op_sel_hi:[0,0,0]
	s_setprio 0
	s_barrier
	s_andn2_b64 vcc, exec, s[82:83]
	s_cbranch_vccnz .LBB0_994
	s_add_u32 s0, s0, 0x180
	s_addc_u32 s1, s1, 0
	s_add_u32 s94, s94, 0x200
	s_addc_u32 s95, s95, 0
	s_mov_b32 s96, 4
